# diff attention: map-1 waves pre-issue the first 16 V-fragment LDS reads of their P.V block at the tail of the previous iteration
# speedup vs baseline: 1.0007x; 1.0007x over previous
.LBB0_640:
	s_cmp_lg_u32 s42, 0
	s_barrier
	s_cselect_b64 s[62:63], -1, 0
	s_and_b64 s[0:1], s[56:57], s[62:63]
	s_andn2_b64 vcc, exec, s[0:1]
	s_cbranch_vccnz .LBB0_642
	s_add_i32 s0, s4, 0x8000
	s_and_b32 s0, s0, 0x18000
	v_add_u32_e32 v1, s0, v222
	s_waitcnt lgkmcnt(8)
	s_nop 0
	v_mfma_f32_32x32x16_bf16 v[52:67], v[96:99], v[100:103], v[52:67]
	v_mfma_f32_32x32x16_bf16 v[52:67], v[92:95], v[104:107], v[52:67]
	v_mfma_f32_32x32x16_bf16 v[52:67], v[88:91], v[108:111], v[52:67]
	v_mfma_f32_32x32x16_bf16 v[52:67], v[84:87], v[112:115], v[52:67]
	ds_read_b64_tr_b16 v[100:101], v1 offset:0x400
	ds_read_b64_tr_b16 v[102:103], v1 offset:0xc00
	ds_read_b64_tr_b16 v[104:105], v1 offset:0x1400
	ds_read_b64_tr_b16 v[106:107], v1 offset:0x1c00
	ds_read_b64_tr_b16 v[108:109], v1 offset:0x2400
	ds_read_b64_tr_b16 v[110:111], v1 offset:0x2c00
	ds_read_b64_tr_b16 v[112:113], v1 offset:0x3400
	ds_read_b64_tr_b16 v[114:115], v1 offset:0x3c00
	s_waitcnt lgkmcnt(8)
	v_mfma_f32_32x32x16_bf16 v[36:51], v[96:99], v[116:119], v[36:51]
	v_mfma_f32_32x32x16_bf16 v[36:51], v[92:95], v[120:123], v[36:51]
	v_mfma_f32_32x32x16_bf16 v[36:51], v[88:91], v[124:127], v[36:51]
	v_mfma_f32_32x32x16_bf16 v[36:51], v[84:87], v[128:131], v[36:51]
	ds_read_b64_tr_b16 v[116:117], v1 offset:0x600
	ds_read_b64_tr_b16 v[118:119], v1 offset:0xe00
	ds_read_b64_tr_b16 v[120:121], v1 offset:0x1600
	ds_read_b64_tr_b16 v[122:123], v1 offset:0x1e00
	ds_read_b64_tr_b16 v[124:125], v1 offset:0x2600
	ds_read_b64_tr_b16 v[126:127], v1 offset:0x2e00
	ds_read_b64_tr_b16 v[128:129], v1 offset:0x3600
	ds_read_b64_tr_b16 v[130:131], v1 offset:0x3e00
	s_waitcnt lgkmcnt(8)
	v_mfma_f32_32x32x16_bf16 v[20:35], v[96:99], v[100:103], v[20:35]
	v_mfma_f32_32x32x16_bf16 v[20:35], v[92:95], v[104:107], v[20:35]
	v_mfma_f32_32x32x16_bf16 v[20:35], v[88:91], v[108:111], v[20:35]
	v_mfma_f32_32x32x16_bf16 v[20:35], v[84:87], v[112:115], v[20:35]
	s_waitcnt lgkmcnt(0)
	v_mfma_f32_32x32x16_bf16 v[4:19], v[96:99], v[116:119], v[4:19]
	v_mfma_f32_32x32x16_bf16 v[4:19], v[92:95], v[120:123], v[4:19]
	v_mfma_f32_32x32x16_bf16 v[4:19], v[88:91], v[124:127], v[4:19]
	v_mfma_f32_32x32x16_bf16 v[4:19], v[84:87], v[128:131], v[4:19]

.Lm1_pre:
	s_add_i32 s0, s4, 0x10000
	s_and_b32 s0, s0, 0x18000
	v_add_u32_e32 v1, s0, v222
	ds_read_b64_tr_b16 v[100:101], v1 offset:0
	ds_read_b64_tr_b16 v[102:103], v1 offset:0x800
	ds_read_b64_tr_b16 v[104:105], v1 offset:0x1000
	ds_read_b64_tr_b16 v[106:107], v1 offset:0x1800
	ds_read_b64_tr_b16 v[108:109], v1 offset:0x2000
	ds_read_b64_tr_b16 v[110:111], v1 offset:0x2800
	ds_read_b64_tr_b16 v[112:113], v1 offset:0x3000
	ds_read_b64_tr_b16 v[114:115], v1 offset:0x3800
	ds_read_b64_tr_b16 v[116:117], v1 offset:0x200
	ds_read_b64_tr_b16 v[118:119], v1 offset:0xa00
	ds_read_b64_tr_b16 v[120:121], v1 offset:0x1200
	ds_read_b64_tr_b16 v[122:123], v1 offset:0x1a00
	ds_read_b64_tr_b16 v[124:125], v1 offset:0x2200
	ds_read_b64_tr_b16 v[126:127], v1 offset:0x2a00
	ds_read_b64_tr_b16 v[128:129], v1 offset:0x3200
	ds_read_b64_tr_b16 v[130:131], v1 offset:0x3a00
	s_branch .LBB0_635
